# stack23 plus the vmcnt wait guarding the CV loads moved to their first consumer (start of the conditional CV tail block)
# speedup vs baseline: 1.0085x; 1.0001x over previous
; #define AT_SBAR() __builtin_amdgcn_sched_barrier(0)
; template <int OFF> DI s16x4 tr_read(int vb) { s16x4 r; asm volatile("ds_read_b64_tr_b16 %0, %1 offset:%2" : "=&v"(r) : "v"(vb), "i"(OFF) : "memory"); return r; }
; template <int D0> DI void pv_one(f32x16& od, int vb, bf16x8 pa0, bf16x8 pa1, bf16x8 pa2, bf16x8 pa3) {
;     const s16x4 l0 = tr_read<v_rd_off(D0, 0, 0)>(vb), h0 = tr_read<v_rd_off(D0, 0, 1)>(vb), l1 = tr_read<v_rd_off(D0, 1, 0)>(vb), h1 = tr_read<v_rd_off(D0, 1, 1)>(vb);
;     const s16x4 l2 = tr_read<v_rd_off(D0, 2, 0)>(vb), h2 = tr_read<v_rd_off(D0, 2, 1)>(vb), l3 = tr_read<v_rd_off(D0, 3, 0)>(vb), h3 = tr_read<v_rd_off(D0, 3, 1)>(vb);
;     asm volatile("s_waitcnt lgkmcnt(0)" ::: "memory"); AT_SBAR();
;     ...
;     od = __builtin_amdgcn_mfma_f32_32x32x16_bf16(AT_PK(l0, h0), pa0, od, 0, 0, 0);
;     od = __builtin_amdgcn_mfma_f32_32x32x16_bf16(AT_PK(l1, h1), pa1, od, 0, 0, 0);
;     od = __builtin_amdgcn_mfma_f32_32x32x16_bf16(AT_PK(l2, h2), pa2, od, 0, 0, 0);
;     od = __builtin_amdgcn_mfma_f32_32x32x16_bf16(AT_PK(l3, h3), pa3, od, 0, 0, 0);
.LBB4_706:
	ds_read_b64_tr_b16 v[214:215], v186 offset:0x600
	ds_read_b64_tr_b16 v[216:217], v186 offset:0x700
	ds_read_b64_tr_b16 v[218:219], v186 offset:0x1600
	ds_read_b64_tr_b16 v[220:221], v186 offset:0x1700
	ds_read_b64_tr_b16 v[222:223], v186 offset:0x2600
	ds_read_b64_tr_b16 v[224:225], v186 offset:0x2700
	ds_read_b64_tr_b16 v[226:227], v186 offset:0x3600
	ds_read_b64_tr_b16 v[228:229], v186 offset:0x3700
	s_waitcnt lgkmcnt(0)
	v_mfma_f32_32x32x16_bf16 v[0:15], v[214:217], v[96:99], v[0:15]
	s_lshl_b32 s2, s64, 14
	s_lshl_b32 s3, s64, 13
	s_sub_i32 s78, s2, s3
	v_mfma_f32_32x32x16_bf16 v[0:15], v[218:221], v[108:111], v[0:15]
	s_andn2_b64 s[2:3], exec, s[34:35]
	s_andn2_b64 vcc, exec, s[34:35]
	v_mfma_f32_32x32x16_bf16 v[0:15], v[222:225], v[100:103], v[0:15]
	v_mfma_f32_32x32x16_bf16 v[0:15], v[226:229], v[104:107], v[0:15]
	s_cbranch_vccnz .LBB4_711
	s_waitcnt vmcnt(3)
	v_med3_f32 v97, v160, -v255, v255
	v_med3_f32 v98, v164, -v255, v255
	v_cvt_scalef32_pk_fp8_f32 v99, v97, v98, s93
	v_med3_f32 v97, v161, -v255, v255
	v_med3_f32 v98, v165, -v255, v255
	v_cvt_scalef32_pk_fp8_f32 v100, v97, v98, s93
	v_med3_f32 v97, v162, -v255, v255
	v_med3_f32 v98, v166, -v255, v255
	s_bitcmp1_b32 s58, 0
	v_cvt_scalef32_pk_fp8_f32 v101, v97, v98, s93
	s_cselect_b32 s8, 0x1100, 0
	v_med3_f32 v97, v163, -v255, v255
	v_med3_f32 v98, v167, -v255, v255
	v_cmp_eq_u32_e32 vcc, 0, v181
	v_add_u32_e32 v96, s8, v191
	v_cvt_scalef32_pk_fp8_f32 v102, v97, v98, s93
	s_and_b64 vcc, exec, vcc
	s_and_b32 s34, s58, 31
	ds_write_b16 v96, v99
	ds_write_b16 v96, v100 offset:68
	ds_write_b16 v96, v101 offset:136
	ds_write_b16 v96, v102 offset:204
	s_cbranch_vccnz .LBB4_735
	s_lshl_b32 s8, s34, 7
	s_lshl_b32 s9, s58, 6
	s_and_b32 s8, s8, 0xf00
	s_and_b32 s9, s9, 64
	s_or_b32 s26, s8, s9
	s_cbranch_execnz .LBB4_710

; #define AT_SBAR() __builtin_amdgcn_sched_barrier(0)
; template <int OFF> DI s16x4 tr_read(int vb) { s16x4 r; asm volatile("ds_read_b64_tr_b16 %0, %1 offset:%2" : "=&v"(r) : "v"(vb), "i"(OFF) : "memory"); return r; }
; template <int D0> DI void pv_one(f32x16& od, int vb, bf16x8 pa0, bf16x8 pa1, bf16x8 pa2, bf16x8 pa3) {
;     const s16x4 l0 = tr_read<v_rd_off(D0, 0, 0)>(vb), h0 = tr_read<v_rd_off(D0, 0, 1)>(vb), l1 = tr_read<v_rd_off(D0, 1, 0)>(vb), h1 = tr_read<v_rd_off(D0, 1, 1)>(vb);
;     const s16x4 l2 = tr_read<v_rd_off(D0, 2, 0)>(vb), h2 = tr_read<v_rd_off(D0, 2, 1)>(vb), l3 = tr_read<v_rd_off(D0, 3, 0)>(vb), h3 = tr_read<v_rd_off(D0, 3, 1)>(vb);
;     asm volatile("s_waitcnt lgkmcnt(0)" ::: "memory"); AT_SBAR();
;     ...
;     od = __builtin_amdgcn_mfma_f32_32x32x16_bf16(AT_PK(l0, h0), pa0, od, 0, 0, 0);
;     od = __builtin_amdgcn_mfma_f32_32x32x16_bf16(AT_PK(l1, h1), pa1, od, 0, 0, 0);
;     od = __builtin_amdgcn_mfma_f32_32x32x16_bf16(AT_PK(l2, h2), pa2, od, 0, 0, 0);
;     od = __builtin_amdgcn_mfma_f32_32x32x16_bf16(AT_PK(l3, h3), pa3, od, 0, 0, 0);
.LBB4_726:
	ds_read_b64_tr_b16 v[216:217], v215 offset:0x600
	ds_read_b64_tr_b16 v[218:219], v215 offset:0x700
	ds_read_b64_tr_b16 v[220:221], v215 offset:0x1600
	ds_read_b64_tr_b16 v[222:223], v215 offset:0x1700
	ds_read_b64_tr_b16 v[224:225], v215 offset:0x2600
	ds_read_b64_tr_b16 v[226:227], v215 offset:0x2700
	ds_read_b64_tr_b16 v[228:229], v215 offset:0x3600
	ds_read_b64_tr_b16 v[230:231], v215 offset:0x3700
	s_waitcnt lgkmcnt(0)
	v_mfma_f32_32x32x16_bf16 v[0:15], v[216:219], v[120:123], v[0:15]
	s_add_i32 s2, s67, 0
	s_mov_b32 s26, 0
	s_andn2_b64 vcc, exec, s[34:35]
	v_mfma_f32_32x32x16_bf16 v[0:15], v[220:223], v[124:127], v[0:15]
	v_mfma_f32_32x32x16_bf16 v[0:15], v[224:227], v[112:115], v[0:15]
	s_andn2_b64 s[2:3], exec, s[34:35]
	v_mfma_f32_32x32x16_bf16 v[0:15], v[228:231], v[116:119], v[0:15]
	s_cbranch_vccnz .LBB4_731
	s_waitcnt vmcnt(3)
	v_med3_f32 v113, v160, -v255, v255
	v_med3_f32 v114, v164, -v255, v255
	v_cvt_scalef32_pk_fp8_f32 v115, v113, v114, s93
	v_med3_f32 v113, v161, -v255, v255
	v_med3_f32 v114, v165, -v255, v255
	v_cvt_scalef32_pk_fp8_f32 v116, v113, v114, s93
	v_med3_f32 v113, v162, -v255, v255
	v_med3_f32 v114, v166, -v255, v255
	s_bitcmp1_b32 s58, 0
	v_cvt_scalef32_pk_fp8_f32 v117, v113, v114, s93
	s_cselect_b32 s8, 0x1100, 0
	v_med3_f32 v113, v163, -v255, v255
	v_med3_f32 v114, v167, -v255, v255
	v_cmp_eq_u32_e32 vcc, 0, v181
	v_add_u32_e32 v112, s8, v191
	v_cvt_scalef32_pk_fp8_f32 v118, v113, v114, s93
	s_and_b64 vcc, exec, vcc
	s_and_b32 s37, s58, 31
	ds_write_b16 v112, v115
	ds_write_b16 v112, v116 offset:68
	ds_write_b16 v112, v117 offset:136
	ds_write_b16 v112, v118 offset:204
	s_cbranch_vccnz .LBB4_736
	s_lshl_b32 s8, s37, 7
	s_lshl_b32 s9, s58, 6
	s_and_b32 s8, s8, 0xf00
	s_and_b32 s9, s9, 64
	s_or_b32 s26, s8, s9
	s_cbranch_execnz .LBB4_730

; #define AT_SBAR() __builtin_amdgcn_sched_barrier(0)
; template <int OFF> DI s16x4 tr_read(int vb) { s16x4 r; asm volatile("ds_read_b64_tr_b16 %0, %1 offset:%2" : "=&v"(r) : "v"(vb), "i"(OFF) : "memory"); return r; }
; template <int D0> DI void pv_one(f32x16& od, int vb, bf16x8 pa0, bf16x8 pa1, bf16x8 pa2, bf16x8 pa3) {
;     const s16x4 l0 = tr_read<v_rd_off(D0, 0, 0)>(vb), h0 = tr_read<v_rd_off(D0, 0, 1)>(vb), l1 = tr_read<v_rd_off(D0, 1, 0)>(vb), h1 = tr_read<v_rd_off(D0, 1, 1)>(vb);
;     const s16x4 l2 = tr_read<v_rd_off(D0, 2, 0)>(vb), h2 = tr_read<v_rd_off(D0, 2, 1)>(vb), l3 = tr_read<v_rd_off(D0, 3, 0)>(vb), h3 = tr_read<v_rd_off(D0, 3, 1)>(vb);
;     asm volatile("s_waitcnt lgkmcnt(0)" ::: "memory"); AT_SBAR();
;     ...
;     od = __builtin_amdgcn_mfma_f32_32x32x16_bf16(AT_PK(l0, h0), pa0, od, 0, 0, 0);
;     od = __builtin_amdgcn_mfma_f32_32x32x16_bf16(AT_PK(l1, h1), pa1, od, 0, 0, 0);
;     od = __builtin_amdgcn_mfma_f32_32x32x16_bf16(AT_PK(l2, h2), pa2, od, 0, 0, 0);
;     od = __builtin_amdgcn_mfma_f32_32x32x16_bf16(AT_PK(l3, h3), pa3, od, 0, 0, 0);
.LBB4_779:
	ds_read_b64_tr_b16 v[218:219], v182 offset:0x600
	ds_read_b64_tr_b16 v[220:221], v182 offset:0x700
	ds_read_b64_tr_b16 v[222:223], v182 offset:0x1600
	ds_read_b64_tr_b16 v[224:225], v182 offset:0x1700
	ds_read_b64_tr_b16 v[226:227], v182 offset:0x2600
	ds_read_b64_tr_b16 v[228:229], v182 offset:0x2700
	ds_read_b64_tr_b16 v[230:231], v182 offset:0x3600
	ds_read_b64_tr_b16 v[232:233], v182 offset:0x3700
	s_waitcnt lgkmcnt(0)
	v_mfma_f32_32x32x16_bf16 v[0:15], v[218:221], v[96:99], v[0:15]
	s_lshl_b32 s2, s15, 14
	s_lshl_b32 s3, s15, 13
	s_sub_i32 s65, s2, s3
	v_mfma_f32_32x32x16_bf16 v[0:15], v[222:225], v[108:111], v[0:15]
	s_andn2_b64 s[2:3], exec, s[22:23]
	s_andn2_b64 vcc, exec, s[22:23]
	v_mfma_f32_32x32x16_bf16 v[0:15], v[226:229], v[100:103], v[0:15]
	v_mfma_f32_32x32x16_bf16 v[0:15], v[230:233], v[104:107], v[0:15]
	s_cbranch_vccnz .LBB4_784
	s_waitcnt vmcnt(3)
	v_med3_f32 v97, v160, -v255, v255
	v_med3_f32 v98, v164, -v255, v255
	v_cvt_scalef32_pk_fp8_f32 v99, v97, v98, s93
	v_med3_f32 v97, v161, -v255, v255
	v_med3_f32 v98, v165, -v255, v255
	v_cvt_scalef32_pk_fp8_f32 v100, v97, v98, s93
	v_med3_f32 v97, v162, -v255, v255
	v_med3_f32 v98, v166, -v255, v255
	s_bitcmp1_b32 s58, 0
	v_cvt_scalef32_pk_fp8_f32 v101, v97, v98, s93
	s_cselect_b32 s8, 0x1100, 0
	v_med3_f32 v97, v163, -v255, v255
	v_med3_f32 v98, v167, -v255, v255
	v_cmp_eq_u32_e32 vcc, 0, v181
	v_add_u32_e32 v96, s8, v195
	v_cvt_scalef32_pk_fp8_f32 v102, v97, v98, s93
	s_and_b64 vcc, exec, vcc
	s_and_b32 s22, s58, 31
	ds_write_b16 v96, v99
	ds_write_b16 v96, v100 offset:68
	ds_write_b16 v96, v101 offset:136
	ds_write_b16 v96, v102 offset:204
	s_cbranch_vccnz .LBB4_808
	s_lshl_b32 s8, s22, 7
	s_lshl_b32 s9, s58, 6
	s_and_b32 s8, s8, 0xf00
	s_and_b32 s9, s9, 64
	s_or_b32 s20, s8, s9
	s_cbranch_execnz .LBB4_783

; #define AT_SBAR() __builtin_amdgcn_sched_barrier(0)
; template <int OFF> DI s16x4 tr_read(int vb) { s16x4 r; asm volatile("ds_read_b64_tr_b16 %0, %1 offset:%2" : "=&v"(r) : "v"(vb), "i"(OFF) : "memory"); return r; }
; template <int D0> DI void pv_one(f32x16& od, int vb, bf16x8 pa0, bf16x8 pa1, bf16x8 pa2, bf16x8 pa3) {
;     const s16x4 l0 = tr_read<v_rd_off(D0, 0, 0)>(vb), h0 = tr_read<v_rd_off(D0, 0, 1)>(vb), l1 = tr_read<v_rd_off(D0, 1, 0)>(vb), h1 = tr_read<v_rd_off(D0, 1, 1)>(vb);
;     const s16x4 l2 = tr_read<v_rd_off(D0, 2, 0)>(vb), h2 = tr_read<v_rd_off(D0, 2, 1)>(vb), l3 = tr_read<v_rd_off(D0, 3, 0)>(vb), h3 = tr_read<v_rd_off(D0, 3, 1)>(vb);
;     asm volatile("s_waitcnt lgkmcnt(0)" ::: "memory"); AT_SBAR();
;     ...
;     od = __builtin_amdgcn_mfma_f32_32x32x16_bf16(AT_PK(l0, h0), pa0, od, 0, 0, 0);
;     od = __builtin_amdgcn_mfma_f32_32x32x16_bf16(AT_PK(l1, h1), pa1, od, 0, 0, 0);
;     od = __builtin_amdgcn_mfma_f32_32x32x16_bf16(AT_PK(l2, h2), pa2, od, 0, 0, 0);
;     od = __builtin_amdgcn_mfma_f32_32x32x16_bf16(AT_PK(l3, h3), pa3, od, 0, 0, 0);
.LBB4_799:
	ds_read_b64_tr_b16 v[220:221], v219 offset:0x600
	ds_read_b64_tr_b16 v[222:223], v219 offset:0x700
	ds_read_b64_tr_b16 v[224:225], v219 offset:0x1600
	ds_read_b64_tr_b16 v[226:227], v219 offset:0x1700
	ds_read_b64_tr_b16 v[228:229], v219 offset:0x2600
	ds_read_b64_tr_b16 v[230:231], v219 offset:0x2700
	ds_read_b64_tr_b16 v[232:233], v219 offset:0x3600
	ds_read_b64_tr_b16 v[234:235], v219 offset:0x3700
	s_waitcnt lgkmcnt(0)
	v_mfma_f32_32x32x16_bf16 v[0:15], v[220:223], v[120:123], v[0:15]
	s_add_i32 s2, s31, 0
	s_mov_b32 s20, 0
	s_andn2_b64 vcc, exec, s[22:23]
	v_mfma_f32_32x32x16_bf16 v[0:15], v[224:227], v[124:127], v[0:15]
	v_mfma_f32_32x32x16_bf16 v[0:15], v[228:231], v[112:115], v[0:15]
	s_andn2_b64 s[2:3], exec, s[22:23]
	v_mfma_f32_32x32x16_bf16 v[0:15], v[232:235], v[116:119], v[0:15]
	s_cbranch_vccnz .LBB4_804
	s_waitcnt vmcnt(3)
	v_med3_f32 v113, v160, -v255, v255
	v_med3_f32 v114, v164, -v255, v255
	v_cvt_scalef32_pk_fp8_f32 v115, v113, v114, s93
	v_med3_f32 v113, v161, -v255, v255
	v_med3_f32 v114, v165, -v255, v255
	v_cvt_scalef32_pk_fp8_f32 v116, v113, v114, s93
	v_med3_f32 v113, v162, -v255, v255
	v_med3_f32 v114, v166, -v255, v255
	s_bitcmp1_b32 s58, 0
	v_cvt_scalef32_pk_fp8_f32 v117, v113, v114, s93
	s_cselect_b32 s8, 0x1100, 0
	v_med3_f32 v113, v163, -v255, v255
	v_med3_f32 v114, v167, -v255, v255
	v_cmp_eq_u32_e32 vcc, 0, v181
	v_add_u32_e32 v112, s8, v195
	v_cvt_scalef32_pk_fp8_f32 v118, v113, v114, s93
	s_and_b64 vcc, exec, vcc
	s_and_b32 s24, s58, 31
	ds_write_b16 v112, v115
	ds_write_b16 v112, v116 offset:68
	ds_write_b16 v112, v117 offset:136
	ds_write_b16 v112, v118 offset:204
	s_cbranch_vccnz .LBB4_809
	s_lshl_b32 s8, s24, 7
	s_lshl_b32 s9, s58, 6
	s_and_b32 s8, s8, 0xf00
	s_and_b32 s9, s9, 64
	s_or_b32 s20, s8, s9
	s_cbranch_execnz .LBB4_803

; #define AT_SBAR() __builtin_amdgcn_sched_barrier(0)
; template <int OFF> DI s16x4 tr_read(int vb) { s16x4 r; asm volatile("ds_read_b64_tr_b16 %0, %1 offset:%2" : "=&v"(r) : "v"(vb), "i"(OFF) : "memory"); return r; }
; template <int D0> DI void pv_one(f32x16& od, int vb, bf16x8 pa0, bf16x8 pa1, bf16x8 pa2, bf16x8 pa3) {
;     const s16x4 l0 = tr_read<v_rd_off(D0, 0, 0)>(vb), h0 = tr_read<v_rd_off(D0, 0, 1)>(vb), l1 = tr_read<v_rd_off(D0, 1, 0)>(vb), h1 = tr_read<v_rd_off(D0, 1, 1)>(vb);
;     const s16x4 l2 = tr_read<v_rd_off(D0, 2, 0)>(vb), h2 = tr_read<v_rd_off(D0, 2, 1)>(vb), l3 = tr_read<v_rd_off(D0, 3, 0)>(vb), h3 = tr_read<v_rd_off(D0, 3, 1)>(vb);
;     asm volatile("s_waitcnt lgkmcnt(0)" ::: "memory"); AT_SBAR();
;     ...
;     od = __builtin_amdgcn_mfma_f32_32x32x16_bf16(AT_PK(l0, h0), pa0, od, 0, 0, 0);
;     od = __builtin_amdgcn_mfma_f32_32x32x16_bf16(AT_PK(l1, h1), pa1, od, 0, 0, 0);
;     od = __builtin_amdgcn_mfma_f32_32x32x16_bf16(AT_PK(l2, h2), pa2, od, 0, 0, 0);
;     od = __builtin_amdgcn_mfma_f32_32x32x16_bf16(AT_PK(l3, h3), pa3, od, 0, 0, 0);
.LBB4_853:
	ds_read_b64_tr_b16 v[214:215], v182 offset:0x600
	ds_read_b64_tr_b16 v[216:217], v182 offset:0x700
	ds_read_b64_tr_b16 v[218:219], v182 offset:0x1600
	ds_read_b64_tr_b16 v[220:221], v182 offset:0x1700
	ds_read_b64_tr_b16 v[222:223], v182 offset:0x2600
	ds_read_b64_tr_b16 v[224:225], v182 offset:0x2700
	ds_read_b64_tr_b16 v[226:227], v182 offset:0x3600
	ds_read_b64_tr_b16 v[228:229], v182 offset:0x3700
	s_waitcnt lgkmcnt(0)
	v_mfma_f32_32x32x16_bf16 v[0:15], v[214:217], v[96:99], v[0:15]
	s_lshl_b32 s2, s57, 14
	s_lshl_b32 s3, s57, 13
	s_sub_i32 s76, s2, s3
	v_mfma_f32_32x32x16_bf16 v[0:15], v[218:221], v[108:111], v[0:15]
	s_andn2_b64 s[2:3], exec, s[30:31]
	s_andn2_b64 vcc, exec, s[30:31]
	v_mfma_f32_32x32x16_bf16 v[0:15], v[222:225], v[100:103], v[0:15]
	v_mfma_f32_32x32x16_bf16 v[0:15], v[226:229], v[104:107], v[0:15]
	s_cbranch_vccnz .LBB4_858
	s_waitcnt vmcnt(3)
	v_med3_f32 v97, v160, -v255, v255
	v_med3_f32 v98, v164, -v255, v255
	v_cvt_scalef32_pk_fp8_f32 v99, v97, v98, s93
	v_med3_f32 v97, v161, -v255, v255
	v_med3_f32 v98, v165, -v255, v255
	v_cvt_scalef32_pk_fp8_f32 v100, v97, v98, s93
	v_med3_f32 v97, v162, -v255, v255
	v_med3_f32 v98, v166, -v255, v255
	s_bitcmp1_b32 s58, 0
	v_cvt_scalef32_pk_fp8_f32 v101, v97, v98, s93
	s_cselect_b32 s8, 0x1100, 0
	v_med3_f32 v97, v163, -v255, v255
	v_med3_f32 v98, v167, -v255, v255
	v_cmp_eq_u32_e32 vcc, 0, v181
	v_add_u32_e32 v96, s8, v190
	v_cvt_scalef32_pk_fp8_f32 v102, v97, v98, s93
	s_and_b64 vcc, exec, vcc
	s_and_b32 s30, s58, 31
	ds_write_b16 v96, v99
	ds_write_b16 v96, v100 offset:68
	ds_write_b16 v96, v101 offset:136
	ds_write_b16 v96, v102 offset:204
	s_cbranch_vccnz .LBB4_882
	s_lshl_b32 s8, s30, 7
	s_lshl_b32 s9, s58, 6
	s_and_b32 s8, s8, 0xf00
	s_and_b32 s9, s9, 64
	s_or_b32 s26, s8, s9
	s_cbranch_execnz .LBB4_857

; #define AT_SBAR() __builtin_amdgcn_sched_barrier(0)
; template <int OFF> DI s16x4 tr_read(int vb) { s16x4 r; asm volatile("ds_read_b64_tr_b16 %0, %1 offset:%2" : "=&v"(r) : "v"(vb), "i"(OFF) : "memory"); return r; }
; template <int D0> DI void pv_one(f32x16& od, int vb, bf16x8 pa0, bf16x8 pa1, bf16x8 pa2, bf16x8 pa3) {
;     const s16x4 l0 = tr_read<v_rd_off(D0, 0, 0)>(vb), h0 = tr_read<v_rd_off(D0, 0, 1)>(vb), l1 = tr_read<v_rd_off(D0, 1, 0)>(vb), h1 = tr_read<v_rd_off(D0, 1, 1)>(vb);
;     const s16x4 l2 = tr_read<v_rd_off(D0, 2, 0)>(vb), h2 = tr_read<v_rd_off(D0, 2, 1)>(vb), l3 = tr_read<v_rd_off(D0, 3, 0)>(vb), h3 = tr_read<v_rd_off(D0, 3, 1)>(vb);
;     asm volatile("s_waitcnt lgkmcnt(0)" ::: "memory"); AT_SBAR();
;     ...
;     od = __builtin_amdgcn_mfma_f32_32x32x16_bf16(AT_PK(l0, h0), pa0, od, 0, 0, 0);
;     od = __builtin_amdgcn_mfma_f32_32x32x16_bf16(AT_PK(l1, h1), pa1, od, 0, 0, 0);
;     od = __builtin_amdgcn_mfma_f32_32x32x16_bf16(AT_PK(l2, h2), pa2, od, 0, 0, 0);
;     od = __builtin_amdgcn_mfma_f32_32x32x16_bf16(AT_PK(l3, h3), pa3, od, 0, 0, 0);
.LBB4_873:
	ds_read_b64_tr_b16 v[216:217], v215 offset:0x600
	ds_read_b64_tr_b16 v[218:219], v215 offset:0x700
	ds_read_b64_tr_b16 v[220:221], v215 offset:0x1600
	ds_read_b64_tr_b16 v[222:223], v215 offset:0x1700
	ds_read_b64_tr_b16 v[224:225], v215 offset:0x2600
	ds_read_b64_tr_b16 v[226:227], v215 offset:0x2700
	ds_read_b64_tr_b16 v[228:229], v215 offset:0x3600
	ds_read_b64_tr_b16 v[230:231], v215 offset:0x3700
	s_waitcnt lgkmcnt(0)
	v_mfma_f32_32x32x16_bf16 v[0:15], v[216:219], v[120:123], v[0:15]
	s_add_i32 s2, s65, 0
	s_mov_b32 s26, 0
	s_andn2_b64 vcc, exec, s[30:31]
	v_mfma_f32_32x32x16_bf16 v[0:15], v[220:223], v[124:127], v[0:15]
	v_mfma_f32_32x32x16_bf16 v[0:15], v[224:227], v[112:115], v[0:15]
	s_andn2_b64 s[2:3], exec, s[30:31]
	v_mfma_f32_32x32x16_bf16 v[0:15], v[228:231], v[116:119], v[0:15]
	s_cbranch_vccnz .LBB4_878
	s_waitcnt vmcnt(3)
	v_med3_f32 v113, v160, -v255, v255
	v_med3_f32 v114, v164, -v255, v255
	v_cvt_scalef32_pk_fp8_f32 v115, v113, v114, s93
	v_med3_f32 v113, v161, -v255, v255
	v_med3_f32 v114, v165, -v255, v255
	v_cvt_scalef32_pk_fp8_f32 v116, v113, v114, s93
	v_med3_f32 v113, v162, -v255, v255
	v_med3_f32 v114, v166, -v255, v255
	s_bitcmp1_b32 s58, 0
	v_cvt_scalef32_pk_fp8_f32 v117, v113, v114, s93
	s_cselect_b32 s8, 0x1100, 0
	v_med3_f32 v113, v163, -v255, v255
	v_med3_f32 v114, v167, -v255, v255
	v_cmp_eq_u32_e32 vcc, 0, v181
	v_add_u32_e32 v112, s8, v190
	v_cvt_scalef32_pk_fp8_f32 v118, v113, v114, s93
	s_and_b64 vcc, exec, vcc
	s_and_b32 s34, s58, 31
	ds_write_b16 v112, v115
	ds_write_b16 v112, v116 offset:68
	ds_write_b16 v112, v117 offset:136
	ds_write_b16 v112, v118 offset:204
	s_cbranch_vccnz .LBB4_883
	s_lshl_b32 s8, s34, 7
	s_lshl_b32 s9, s58, 6
	s_and_b32 s8, s8, 0xf00
	s_and_b32 s9, s9, 64
	s_or_b32 s26, s8, s9
	s_cbranch_execnz .LBB4_877

; #define AT_SBAR() __builtin_amdgcn_sched_barrier(0)
; template <int OFF> DI s16x4 tr_read(int vb) { s16x4 r; asm volatile("ds_read_b64_tr_b16 %0, %1 offset:%2" : "=&v"(r) : "v"(vb), "i"(OFF) : "memory"); return r; }
; template <int D0> DI void pv_one(f32x16& od, int vb, bf16x8 pa0, bf16x8 pa1, bf16x8 pa2, bf16x8 pa3) {
;     const s16x4 l0 = tr_read<v_rd_off(D0, 0, 0)>(vb), h0 = tr_read<v_rd_off(D0, 0, 1)>(vb), l1 = tr_read<v_rd_off(D0, 1, 0)>(vb), h1 = tr_read<v_rd_off(D0, 1, 1)>(vb);
;     const s16x4 l2 = tr_read<v_rd_off(D0, 2, 0)>(vb), h2 = tr_read<v_rd_off(D0, 2, 1)>(vb), l3 = tr_read<v_rd_off(D0, 3, 0)>(vb), h3 = tr_read<v_rd_off(D0, 3, 1)>(vb);
;     asm volatile("s_waitcnt lgkmcnt(0)" ::: "memory"); AT_SBAR();
;     ...
;     od = __builtin_amdgcn_mfma_f32_32x32x16_bf16(AT_PK(l0, h0), pa0, od, 0, 0, 0);
;     od = __builtin_amdgcn_mfma_f32_32x32x16_bf16(AT_PK(l1, h1), pa1, od, 0, 0, 0);
;     od = __builtin_amdgcn_mfma_f32_32x32x16_bf16(AT_PK(l2, h2), pa2, od, 0, 0, 0);
;     od = __builtin_amdgcn_mfma_f32_32x32x16_bf16(AT_PK(l3, h3), pa3, od, 0, 0, 0);
.LBB4_927:
	ds_read_b64_tr_b16 v[218:219], v182 offset:0x600
	ds_read_b64_tr_b16 v[220:221], v182 offset:0x700
	ds_read_b64_tr_b16 v[222:223], v182 offset:0x1600
	ds_read_b64_tr_b16 v[224:225], v182 offset:0x1700
	ds_read_b64_tr_b16 v[226:227], v182 offset:0x2600
	ds_read_b64_tr_b16 v[228:229], v182 offset:0x2700
	ds_read_b64_tr_b16 v[230:231], v182 offset:0x3600
	ds_read_b64_tr_b16 v[232:233], v182 offset:0x3700
	s_waitcnt lgkmcnt(0)
	v_mfma_f32_32x32x16_bf16 v[0:15], v[218:221], v[96:99], v[0:15]
	s_lshl_b32 s2, s15, 14
	s_lshl_b32 s3, s15, 13
	s_sub_i32 s54, s2, s3
	v_mfma_f32_32x32x16_bf16 v[0:15], v[222:225], v[108:111], v[0:15]
	s_andn2_b64 s[2:3], exec, s[22:23]
	s_andn2_b64 vcc, exec, s[22:23]
	v_mfma_f32_32x32x16_bf16 v[0:15], v[226:229], v[100:103], v[0:15]
	v_mfma_f32_32x32x16_bf16 v[0:15], v[230:233], v[104:107], v[0:15]
	s_cbranch_vccnz .LBB4_932
	s_waitcnt vmcnt(3)
	v_med3_f32 v97, v160, -v255, v255
	v_med3_f32 v98, v164, -v255, v255
	v_cvt_scalef32_pk_fp8_f32 v99, v97, v98, s93
	v_med3_f32 v97, v161, -v255, v255
	v_med3_f32 v98, v165, -v255, v255
	v_cvt_scalef32_pk_fp8_f32 v100, v97, v98, s93
	v_med3_f32 v97, v162, -v255, v255
	v_med3_f32 v98, v166, -v255, v255
	s_bitcmp1_b32 s58, 0
	v_cvt_scalef32_pk_fp8_f32 v101, v97, v98, s93
	s_cselect_b32 s8, 0x1100, 0
	v_med3_f32 v97, v163, -v255, v255
	v_med3_f32 v98, v167, -v255, v255
	v_cmp_eq_u32_e32 vcc, 0, v181
	v_add_u32_e32 v96, s8, v195
	v_cvt_scalef32_pk_fp8_f32 v102, v97, v98, s93
	s_and_b64 vcc, exec, vcc
	s_and_b32 s22, s58, 31
	ds_write_b16 v96, v99
	ds_write_b16 v96, v100 offset:68
	ds_write_b16 v96, v101 offset:136
	ds_write_b16 v96, v102 offset:204
	s_cbranch_vccnz .LBB4_956
	s_lshl_b32 s8, s22, 7
	s_lshl_b32 s9, s58, 6
	s_and_b32 s8, s8, 0xf00
	s_and_b32 s9, s9, 64
	s_or_b32 s18, s8, s9
	s_cbranch_execnz .LBB4_931

; #define AT_SBAR() __builtin_amdgcn_sched_barrier(0)
; template <int OFF> DI s16x4 tr_read(int vb) { s16x4 r; asm volatile("ds_read_b64_tr_b16 %0, %1 offset:%2" : "=&v"(r) : "v"(vb), "i"(OFF) : "memory"); return r; }
; template <int D0> DI void pv_one(f32x16& od, int vb, bf16x8 pa0, bf16x8 pa1, bf16x8 pa2, bf16x8 pa3) {
;     const s16x4 l0 = tr_read<v_rd_off(D0, 0, 0)>(vb), h0 = tr_read<v_rd_off(D0, 0, 1)>(vb), l1 = tr_read<v_rd_off(D0, 1, 0)>(vb), h1 = tr_read<v_rd_off(D0, 1, 1)>(vb);
;     const s16x4 l2 = tr_read<v_rd_off(D0, 2, 0)>(vb), h2 = tr_read<v_rd_off(D0, 2, 1)>(vb), l3 = tr_read<v_rd_off(D0, 3, 0)>(vb), h3 = tr_read<v_rd_off(D0, 3, 1)>(vb);
;     asm volatile("s_waitcnt lgkmcnt(0)" ::: "memory"); AT_SBAR();
;     ...
;     od = __builtin_amdgcn_mfma_f32_32x32x16_bf16(AT_PK(l0, h0), pa0, od, 0, 0, 0);
;     od = __builtin_amdgcn_mfma_f32_32x32x16_bf16(AT_PK(l1, h1), pa1, od, 0, 0, 0);
;     od = __builtin_amdgcn_mfma_f32_32x32x16_bf16(AT_PK(l2, h2), pa2, od, 0, 0, 0);
;     od = __builtin_amdgcn_mfma_f32_32x32x16_bf16(AT_PK(l3, h3), pa3, od, 0, 0, 0);
.LBB4_947:
	ds_read_b64_tr_b16 v[220:221], v219 offset:0x600
	ds_read_b64_tr_b16 v[222:223], v219 offset:0x700
	ds_read_b64_tr_b16 v[224:225], v219 offset:0x1600
	ds_read_b64_tr_b16 v[226:227], v219 offset:0x1700
	ds_read_b64_tr_b16 v[228:229], v219 offset:0x2600
	ds_read_b64_tr_b16 v[230:231], v219 offset:0x2700
	ds_read_b64_tr_b16 v[232:233], v219 offset:0x3600
	ds_read_b64_tr_b16 v[234:235], v219 offset:0x3700
	s_waitcnt lgkmcnt(0)
	v_mfma_f32_32x32x16_bf16 v[0:15], v[220:223], v[120:123], v[0:15]
	s_add_i32 s2, s31, 0
	s_mov_b32 s18, 0
	s_andn2_b64 vcc, exec, s[22:23]
	v_mfma_f32_32x32x16_bf16 v[0:15], v[224:227], v[124:127], v[0:15]
	v_mfma_f32_32x32x16_bf16 v[0:15], v[228:231], v[112:115], v[0:15]
	s_andn2_b64 s[2:3], exec, s[22:23]
	v_mfma_f32_32x32x16_bf16 v[0:15], v[232:235], v[116:119], v[0:15]
	s_cbranch_vccnz .LBB4_952
	s_waitcnt vmcnt(3)
	v_med3_f32 v113, v160, -v255, v255
	v_med3_f32 v114, v164, -v255, v255
	v_cvt_scalef32_pk_fp8_f32 v115, v113, v114, s93
	v_med3_f32 v113, v161, -v255, v255
	v_med3_f32 v114, v165, -v255, v255
	v_cvt_scalef32_pk_fp8_f32 v116, v113, v114, s93
	v_med3_f32 v113, v162, -v255, v255
	v_med3_f32 v114, v166, -v255, v255
	s_bitcmp1_b32 s58, 0
	v_cvt_scalef32_pk_fp8_f32 v117, v113, v114, s93
	s_cselect_b32 s8, 0x1100, 0
	v_med3_f32 v113, v163, -v255, v255
	v_med3_f32 v114, v167, -v255, v255
	v_cmp_eq_u32_e32 vcc, 0, v181
	v_add_u32_e32 v112, s8, v195
	v_cvt_scalef32_pk_fp8_f32 v118, v113, v114, s93
	s_and_b64 vcc, exec, vcc
	s_and_b32 s24, s58, 31
	ds_write_b16 v112, v115
	ds_write_b16 v112, v116 offset:68
	ds_write_b16 v112, v117 offset:136
	ds_write_b16 v112, v118 offset:204
	s_cbranch_vccnz .LBB4_957
	s_lshl_b32 s8, s24, 7
	s_lshl_b32 s9, s58, 6
	s_and_b32 s8, s8, 0xf00
	s_and_b32 s9, s9, 64
	s_or_b32 s18, s8, s9
	s_cbranch_execnz .LBB4_951
